# P11 epilogue de-serialised: residual rows and final-norm weights loaded up front into dedicated registers; per-quarter load/vmcnt(0)/store ladder removed
# baseline (speedup 1.0000x reference)
;     ...
;     asm volatile("v_mbcnt_lo_u32_b32 %0, -1, 0\n\tv_mbcnt_hi_u32_b32 %0, -1, %0" : "=v"(lane)); asm volatile("" : "+s"(tbase));
; #pragma unroll
;     for (int j = 0; j < PE_NT; ++j) {
;         const int t = tbase + j;
;         float ss = 0.f; f32x4 xo[4];
;         { const v4u* xrow = (const v4u*)((const bf16*)(ws + WS_XB) + (size_t)t * 1024 + 16 * lane); const v4u xa = xrow[0], xc = xrow[1];
;           xo[0] = (f32x4){bflo(xa.x), bfhi(xa.x), bflo(xa.y), bfhi(xa.y)}; xo[1] = (f32x4){bflo(xa.z), bfhi(xa.z), bflo(xa.w), bfhi(xa.w)};
;           xo[2] = (f32x4){bflo(xc.x), bfhi(xc.x), bflo(xc.y), bfhi(xc.y)}; xo[3] = (f32x4){bflo(xc.z), bfhi(xc.z), bflo(xc.w), bfhi(xc.w)}; }
; #pragma unroll
;         for (int i = 0; i < 4; ++i) { xo[i].x += acc[j][2 * i].x; xo[i].y += acc[j][2 * i].y; xo[i].z += acc[j][2 * i + 1].x; xo[i].w += acc[j][2 * i + 1].y;
;             ss += (xo[i].x * xo[i].x + xo[i].y * xo[i].y) + (xo[i].z * xo[i].z + xo[i].w * xo[i].w); }
;         const float rstd3 = rsqrtf(wave_sum(ss) * (1.0f / 1024.0f) + 1e-6f);
;         float* orow = dstbase + (size_t)t * 1024 + 16 * lane;
; #pragma unroll
;         for (int i = 0; i < 4; ++i) { const f32x4 w = ((const f32x4*)(P.norm_final_w + 16 * lane))[i];
;             ((f32x4*)orow)[i] = (f32x4){xo[i].x * rstd3 * w.x, xo[i].y * rstd3 * w.y, xo[i].z * rstd3 * w.z, xo[i].w * rstd3 * w.w}; }
.LBB0_2678:
	s_cmp_eq_u32 s7, 0
	s_waitcnt vmcnt(0)
	s_cselect_b64 s[4:5], -1, 0
	s_cmp_eq_u32 s7, 1
	s_waitcnt vmcnt(0)
	s_cselect_b64 s[2:3], -1, 0
	s_cmp_eq_u32 s7, 2
	s_waitcnt vmcnt(0)
	s_cselect_b64 s[0:1], -1, 0
	s_cmp_eq_u32 s7, 3
	v_mbcnt_lo_u32_b32 v48, -1, 0
	v_mbcnt_hi_u32_b32 v48, -1, v48
	s_cselect_b64 vcc, -1, 0
	v_lshlrev_b32_e32 v70, 4, v48
	v_ashrrev_i32_e32 v71, 31, v70
	s_ashr_i32 s85, s84, 31
	v_lshl_add_u64 v[72:73], v[70:71], 1, s[80:81]
	s_lshl_b64 s[6:7], s[84:85], 11
	v_lshl_add_u64 v[82:83], v[72:73], 0, s[6:7]
	global_load_dwordx4 v[74:77], v[82:83], off
	global_load_dwordx4 v[78:81], v[82:83], off offset:16
	global_load_dwordx4 v[156:159], v[82:83], off offset:2048
	global_load_dwordx4 v[160:163], v[82:83], off offset:2064
	s_mov_b64 s[98:99], 0x1000
	v_lshl_add_u64 v[188:189], v[82:83], 0, s[98:99]
	global_load_dwordx4 v[164:167], v[188:189], off
	global_load_dwordx4 v[168:171], v[188:189], off offset:16
	global_load_dwordx4 v[172:175], v[188:189], off offset:2048
	global_load_dwordx4 v[176:179], v[188:189], off offset:2064
	v_cndmask_b32_e64 v48, 0, v121, s[4:5]
	v_readlane_b32 s4, v254, 58
	v_lshlrev_b64 v[86:87], 2, v[70:71]
	v_readlane_b32 s8, v254, 62
	v_readlane_b32 s9, v254, 63
	v_pk_fma_f32 v[60:61], v[102:103], v[48:49], v[60:61] op_sel_hi:[1,0,1]
	v_pk_fma_f32 v[58:59], v[104:105], v[48:49], v[58:59] op_sel_hi:[1,0,1]
	v_lshl_add_u64 v[70:71], s[8:9], 0, v[86:87]
	global_load_dwordx4 v[140:143], v[70:71], off
	global_load_dwordx4 v[144:147], v[70:71], off offset:16
	global_load_dwordx4 v[148:151], v[70:71], off offset:32
	global_load_dwordx4 v[152:155], v[70:71], off offset:48
	v_pk_fma_f32 v[56:57], v[2:3], v[48:49], v[56:57] op_sel_hi:[1,0,1]
	v_pk_fma_f32 v[54:55], v[0:1], v[48:49], v[54:55] op_sel_hi:[1,0,1]
	v_pk_fma_f32 v[64:65], v[98:99], v[48:49], v[64:65] op_sel_hi:[1,0,1]
	v_pk_fma_f32 v[62:63], v[100:101], v[48:49], v[62:63] op_sel_hi:[1,0,1]
	v_pk_fma_f32 v[68:69], v[94:95], v[48:49], v[68:69] op_sel_hi:[1,0,1]
	v_pk_fma_f32 v[66:67], v[96:97], v[48:49], v[66:67] op_sel_hi:[1,0,1]
	v_readlane_b32 s5, v254, 59
	s_mov_b32 s8, 0x800000
	v_readlane_b32 s6, v254, 60
	v_readlane_b32 s7, v254, 61
	v_readlane_b32 s10, v255, 0
	v_readlane_b32 s11, v255, 1
	s_lshl_b64 s[6:7], s[84:85], 12
	s_waitcnt vmcnt(11)
	v_lshlrev_b32_e32 v88, 16, v74
	v_and_b32_e32 v89, 0xffff0000, v74
	v_lshlrev_b32_e32 v74, 16, v75
	v_and_b32_e32 v75, 0xffff0000, v75
	v_lshlrev_b32_e32 v90, 16, v76
	v_and_b32_e32 v91, 0xffff0000, v76
	v_lshlrev_b32_e32 v76, 16, v77
	v_and_b32_e32 v77, 0xffff0000, v77
	s_waitcnt vmcnt(10)
	v_lshlrev_b32_e32 v92, 16, v78
	v_and_b32_e32 v93, 0xffff0000, v78
	v_lshlrev_b32_e32 v78, 16, v79
	v_and_b32_e32 v79, 0xffff0000, v79
	v_pk_add_f32 v[88:89], v[54:55], v[88:89]
	v_pk_add_f32 v[56:57], v[56:57], v[74:75]
	v_pk_add_f32 v[74:75], v[58:59], v[90:91]
	v_pk_add_f32 v[60:61], v[60:61], v[76:77]
	v_lshlrev_b32_e32 v106, 16, v80
	v_and_b32_e32 v107, 0xffff0000, v80
	v_lshlrev_b32_e32 v80, 16, v81
	v_and_b32_e32 v81, 0xffff0000, v81
	v_pk_add_f32 v[62:63], v[62:63], v[92:93]
	v_pk_add_f32 v[64:65], v[64:65], v[78:79]
	v_pk_mul_f32 v[54:55], v[88:89], v[88:89]
	v_pk_mul_f32 v[58:59], v[56:57], v[56:57]
	v_pk_mul_f32 v[76:77], v[74:75], v[74:75]
	v_pk_mul_f32 v[78:79], v[60:61], v[60:61]
	v_pk_add_f32 v[66:67], v[66:67], v[106:107]
	v_pk_add_f32 v[68:69], v[68:69], v[80:81]
	v_pk_mul_f32 v[80:81], v[62:63], v[62:63]
	v_pk_mul_f32 v[90:91], v[64:65], v[64:65]
	v_add_f32_e32 v48, v78, v79
	v_add_f32_e32 v76, v76, v77
	v_add_f32_e32 v58, v58, v59
	v_add_f32_e32 v54, v54, v55
	v_pk_mul_f32 v[92:93], v[66:67], v[66:67]
	v_pk_mul_f32 v[106:107], v[68:69], v[68:69]
	v_add_f32_e32 v55, v90, v91
	v_add_f32_e32 v59, v80, v81
	v_add_f32_e32 v48, v76, v48
	v_add_f32_e32 v54, v54, v58
	v_add_f32_e32 v77, v106, v107
	v_add_f32_e32 v78, v92, v93
	v_add_f32_e32 v55, v59, v55
	v_add_f32_e32 v48, v54, v48
	v_add_f32_e32 v58, v78, v77
	v_add_f32_e32 v48, v48, v55
	v_add_f32_e32 v48, v58, v48
	s_nop 1
	v_add_f32_dpp v48, v48, v48 quad_perm:[1,0,3,2] row_mask:0xf bank_mask:0xf bound_ctrl:1
	s_nop 1
	v_add_f32_dpp v48, v48, v48 quad_perm:[2,3,0,1] row_mask:0xf bank_mask:0xf bound_ctrl:1
	s_nop 1
	v_add_f32_dpp v48, v48, v48 row_half_mirror row_mask:0xf bank_mask:0xf bound_ctrl:1
	s_nop 1
	v_add_f32_dpp v48, v48, v48 row_mirror row_mask:0xf bank_mask:0xf bound_ctrl:1
	v_mov_b32_e32 v54, v48
	s_nop 1
	v_permlane16_swap_b32_e32 v48, v54
	v_add_f32 v48, v48, v54
	s_nop 1
	s_nop 0
	v_mov_b32_e32 v54, v48
	s_nop 1
	v_permlane32_swap_b32_e32 v48, v54
	v_add_f32 v48, v48, v54
	s_nop 0
	v_fmamk_f32 v48, v48, 0x3a800000, v110
	v_mul_f32_e32 v54, 0x4b800000, v48
	v_cmp_gt_f32_e64 s[4:5], s8, v48
	s_nop 1
	v_cndmask_b32_e64 v48, v48, v54, s[4:5]
	v_rsq_f32_e32 v48, v48
	v_lshl_add_u64 v[54:55], s[10:11], 0, v[86:87]
	v_lshl_add_u64 v[76:77], v[54:55], 0, s[6:7]
	v_mul_f32_e32 v58, 0x45800000, v48
	v_cndmask_b32_e64 v48, v48, v58, s[4:5]
	v_pk_mul_f32 v[78:79], v[88:89], v[48:49] op_sel_hi:[1,0]
	v_pk_mul_f32 v[56:57], v[56:57], v[48:49] op_sel_hi:[1,0]
	v_pk_mul_f32 v[60:61], v[60:61], v[48:49] op_sel_hi:[1,0]
	s_waitcnt vmcnt(0)
;     ...
; #pragma unroll
;     for (int j = 0; j < PE_NT; ++j) {
;         const int t = tbase + j;
;         float ss = 0.f; f32x4 xo[4];
;         { const v4u* xrow = (const v4u*)((const bf16*)(ws + WS_XB) + (size_t)t * 1024 + 16 * lane); const v4u xa = xrow[0], xc = xrow[1];
;           xo[0] = (f32x4){bflo(xa.x), bfhi(xa.x), bflo(xa.y), bfhi(xa.y)}; xo[1] = (f32x4){bflo(xa.z), bfhi(xa.z), bflo(xa.w), bfhi(xa.w)};
;           xo[2] = (f32x4){bflo(xc.x), bfhi(xc.x), bflo(xc.y), bfhi(xc.y)}; xo[3] = (f32x4){bflo(xc.z), bfhi(xc.z), bflo(xc.w), bfhi(xc.w)}; }
; #pragma unroll
;         for (int i = 0; i < 4; ++i) { xo[i].x += acc[j][2 * i].x; xo[i].y += acc[j][2 * i].y; xo[i].z += acc[j][2 * i + 1].x; xo[i].w += acc[j][2 * i + 1].y;
;             ss += (xo[i].x * xo[i].x + xo[i].y * xo[i].y) + (xo[i].z * xo[i].z + xo[i].w * xo[i].w); }
;         const float rstd3 = rsqrtf(wave_sum(ss) * (1.0f / 1024.0f) + 1e-6f);
;         float* orow = dstbase + (size_t)t * 1024 + 16 * lane;
; #pragma unroll
;         for (int i = 0; i < 4; ++i) { const f32x4 w = ((const f32x4*)(P.norm_final_w + 16 * lane))[i];
;             ((f32x4*)orow)[i] = (f32x4){xo[i].x * rstd3 * w.x, xo[i].y * rstd3 * w.y, xo[i].z * rstd3 * w.z, xo[i].w * rstd3 * w.w}; }
	v_pk_mul_f32 v[58:59], v[142:143], v[56:57]
	v_pk_mul_f32 v[56:57], v[140:141], v[78:79]
	global_store_dwordx4 v[76:77], v[56:59], off
	v_pk_mul_f32 v[74:75], v[74:75], v[48:49] op_sel_hi:[1,0]
	v_pk_mul_f32 v[62:63], v[62:63], v[48:49] op_sel_hi:[1,0]
	s_add_i32 s4, s84, 1
	s_ashr_i32 s5, s4, 31
	s_lshl_b64 s[6:7], s[4:5], 11
	s_lshl_b64 s[4:5], s[4:5], 12
	v_pk_mul_f32 v[56:57], v[144:145], v[74:75]
	v_pk_mul_f32 v[58:59], v[146:147], v[60:61]
	global_store_dwordx4 v[76:77], v[56:59], off offset:16
	v_pk_mul_f32 v[60:61], v[64:65], v[48:49] op_sel_hi:[1,0]
	v_lshl_add_u64 v[64:65], v[72:73], 0, s[6:7]
	v_readlane_b32 s6, v254, 24
	v_pk_mul_f32 v[56:57], v[148:149], v[62:63]
	v_pk_mul_f32 v[58:59], v[150:151], v[60:61]
	global_store_dwordx4 v[76:77], v[56:59], off offset:32
	v_pk_mul_f32 v[60:61], v[68:69], v[48:49] op_sel_hi:[1,0]
	v_pk_mul_f32 v[62:63], v[66:67], v[48:49] op_sel_hi:[1,0]
	v_cndmask_b32_e64 v48, 0, v120, s[2:3]
	v_pk_fma_f32 v[42:43], v[102:103], v[48:49], v[42:43] op_sel_hi:[1,0,1]
	v_pk_fma_f32 v[40:41], v[104:105], v[48:49], v[40:41] op_sel_hi:[1,0,1]
	v_pk_fma_f32 v[38:39], v[2:3], v[48:49], v[38:39] op_sel_hi:[1,0,1]
	v_pk_fma_f32 v[36:37], v[0:1], v[48:49], v[36:37] op_sel_hi:[1,0,1]
	v_pk_fma_f32 v[52:53], v[94:95], v[48:49], v[52:53] op_sel_hi:[1,0,1]
	v_pk_fma_f32 v[46:47], v[98:99], v[48:49], v[46:47] op_sel_hi:[1,0,1]
	v_pk_fma_f32 v[44:45], v[100:101], v[48:49], v[44:45] op_sel_hi:[1,0,1]
	v_pk_fma_f32 v[50:51], v[96:97], v[48:49], v[50:51] op_sel_hi:[1,0,1]
	v_pk_mul_f32 v[56:57], v[152:153], v[62:63]
	v_pk_mul_f32 v[58:59], v[154:155], v[60:61]
	global_store_dwordx4 v[76:77], v[56:59], off offset:48
	s_nop 0
	v_lshlrev_b32_e32 v68, 16, v156
	v_and_b32_e32 v69, 0xffff0000, v156
	v_lshlrev_b32_e32 v56, 16, v157
	v_and_b32_e32 v57, 0xffff0000, v157
	v_lshlrev_b32_e32 v74, 16, v158
	v_and_b32_e32 v75, 0xffff0000, v158
	v_lshlrev_b32_e32 v58, 16, v159
	v_and_b32_e32 v59, 0xffff0000, v159
	v_lshlrev_b32_e32 v76, 16, v160
	v_and_b32_e32 v77, 0xffff0000, v160
	v_lshlrev_b32_e32 v60, 16, v161
	v_and_b32_e32 v61, 0xffff0000, v161
	v_lshlrev_b32_e32 v78, 16, v162
	v_and_b32_e32 v79, 0xffff0000, v162
	v_lshlrev_b32_e32 v62, 16, v163
	v_and_b32_e32 v63, 0xffff0000, v163
	v_pk_add_f32 v[36:37], v[36:37], v[68:69]
	v_pk_add_f32 v[38:39], v[38:39], v[56:57]
	v_pk_add_f32 v[40:41], v[40:41], v[74:75]
	v_pk_add_f32 v[42:43], v[42:43], v[58:59]
	v_pk_add_f32 v[44:45], v[44:45], v[76:77]
	v_pk_add_f32 v[46:47], v[46:47], v[60:61]
	v_pk_add_f32 v[52:53], v[52:53], v[62:63]
	v_pk_mul_f32 v[56:57], v[36:37], v[36:37]
	v_pk_mul_f32 v[58:59], v[38:39], v[38:39]
	v_pk_mul_f32 v[60:61], v[40:41], v[40:41]
	v_pk_mul_f32 v[62:63], v[42:43], v[42:43]
	v_pk_add_f32 v[50:51], v[50:51], v[78:79]
	v_pk_mul_f32 v[68:69], v[44:45], v[44:45]
	v_pk_mul_f32 v[74:75], v[46:47], v[46:47]
	v_add_f32_e32 v48, v62, v63
	v_add_f32_e32 v60, v60, v61
	v_add_f32_e32 v58, v58, v59
	v_add_f32_e32 v56, v56, v57
	v_pk_mul_f32 v[76:77], v[50:51], v[50:51]
	v_pk_mul_f32 v[78:79], v[52:53], v[52:53]
	v_add_f32_e32 v57, v74, v75
	v_add_f32_e32 v59, v68, v69
	v_add_f32_e32 v48, v60, v48
	v_add_f32_e32 v56, v56, v58
	v_add_f32_e32 v61, v78, v79
	v_add_f32_e32 v62, v76, v77
	v_add_f32_e32 v57, v59, v57
	v_add_f32_e32 v48, v56, v48
	v_add_f32_e32 v58, v62, v61
	v_add_f32_e32 v48, v48, v57
	v_add_f32_e32 v48, v58, v48
	s_nop 1
	v_add_f32_dpp v48, v48, v48 quad_perm:[1,0,3,2] row_mask:0xf bank_mask:0xf bound_ctrl:1
	s_nop 1
	v_add_f32_dpp v48, v48, v48 quad_perm:[2,3,0,1] row_mask:0xf bank_mask:0xf bound_ctrl:1
	s_nop 1
	v_add_f32_dpp v48, v48, v48 row_half_mirror row_mask:0xf bank_mask:0xf bound_ctrl:1
	s_nop 1
	v_add_f32_dpp v48, v48, v48 row_mirror row_mask:0xf bank_mask:0xf bound_ctrl:1
	v_mov_b32_e32 v56, v48
	s_nop 1
	v_permlane16_swap_b32_e32 v48, v56
	v_add_f32 v48, v48, v56
	s_nop 1
	s_nop 0
	v_mov_b32_e32 v56, v48
	s_nop 1
	v_permlane32_swap_b32_e32 v48, v56
	v_add_f32 v48, v48, v56
	s_nop 0
	v_fmamk_f32 v48, v48, 0x3a800000, v110
	v_mul_f32_e32 v56, 0x4b800000, v48
	v_cmp_gt_f32_e64 s[2:3], s8, v48
	s_nop 1
	v_cndmask_b32_e64 v48, v48, v56, s[2:3]
	v_rsq_f32_e32 v48, v48
	v_lshl_add_u64 v[56:57], v[54:55], 0, s[4:5]
	v_mul_f32_e32 v58, 0x45800000, v48
	v_cndmask_b32_e64 v48, v48, v58, s[2:3]
	v_pk_mul_f32 v[36:37], v[36:37], v[48:49] op_sel_hi:[1,0]
	v_pk_mul_f32 v[38:39], v[38:39], v[48:49] op_sel_hi:[1,0]
	v_pk_mul_f32 v[36:37], v[140:141], v[36:37]
	v_pk_mul_f32 v[38:39], v[142:143], v[38:39]
	global_store_dwordx4 v[56:57], v[36:39], off
	v_pk_mul_f32 v[42:43], v[42:43], v[48:49] op_sel_hi:[1,0]
	v_pk_mul_f32 v[40:41], v[40:41], v[48:49] op_sel_hi:[1,0]
	s_add_i32 s2, s84, 2
	s_ashr_i32 s3, s2, 31
	s_lshl_b64 s[4:5], s[2:3], 11
	s_lshl_b64 s[2:3], s[2:3], 12
	v_pk_mul_f32 v[36:37], v[144:145], v[40:41]
	v_pk_mul_f32 v[38:39], v[146:147], v[42:43]
	global_store_dwordx4 v[56:57], v[36:39], off offset:16
	v_pk_mul_f32 v[40:41], v[46:47], v[48:49] op_sel_hi:[1,0]
	v_pk_mul_f32 v[42:43], v[44:45], v[48:49] op_sel_hi:[1,0]
	v_lshl_add_u64 v[44:45], v[72:73], 0, s[4:5]
	v_pk_mul_f32 v[36:37], v[148:149], v[42:43]
	v_pk_mul_f32 v[38:39], v[150:151], v[40:41]
	global_store_dwordx4 v[56:57], v[36:39], off offset:32
	v_pk_mul_f32 v[40:41], v[52:53], v[48:49] op_sel_hi:[1,0]
	v_pk_mul_f32 v[42:43], v[50:51], v[48:49] op_sel_hi:[1,0]
	v_cndmask_b32_e64 v48, 0, v119, s[0:1]
	v_pk_fma_f32 v[26:27], v[102:103], v[48:49], v[26:27] op_sel_hi:[1,0,1]
	v_pk_fma_f32 v[24:25], v[104:105], v[48:49], v[24:25] op_sel_hi:[1,0,1]
	v_pk_fma_f32 v[22:23], v[2:3], v[48:49], v[22:23] op_sel_hi:[1,0,1]
	v_pk_fma_f32 v[20:21], v[0:1], v[48:49], v[20:21] op_sel_hi:[1,0,1]
;     ...
; #pragma unroll
;     for (int j = 0; j < PE_NT; ++j) {
;         const int t = tbase + j;
;         float ss = 0.f; f32x4 xo[4];
;         { const v4u* xrow = (const v4u*)((const bf16*)(ws + WS_XB) + (size_t)t * 1024 + 16 * lane); const v4u xa = xrow[0], xc = xrow[1];
;           xo[0] = (f32x4){bflo(xa.x), bfhi(xa.x), bflo(xa.y), bfhi(xa.y)}; xo[1] = (f32x4){bflo(xa.z), bfhi(xa.z), bflo(xa.w), bfhi(xa.w)};
;           xo[2] = (f32x4){bflo(xc.x), bfhi(xc.x), bflo(xc.y), bfhi(xc.y)}; xo[3] = (f32x4){bflo(xc.z), bfhi(xc.z), bflo(xc.w), bfhi(xc.w)}; }
; #pragma unroll
;         for (int i = 0; i < 4; ++i) { xo[i].x += acc[j][2 * i].x; xo[i].y += acc[j][2 * i].y; xo[i].z += acc[j][2 * i + 1].x; xo[i].w += acc[j][2 * i + 1].y;
;             ss += (xo[i].x * xo[i].x + xo[i].y * xo[i].y) + (xo[i].z * xo[i].z + xo[i].w * xo[i].w); }
;         const float rstd3 = rsqrtf(wave_sum(ss) * (1.0f / 1024.0f) + 1e-6f);
;         float* orow = dstbase + (size_t)t * 1024 + 16 * lane;
; #pragma unroll
;         for (int i = 0; i < 4; ++i) { const f32x4 w = ((const f32x4*)(P.norm_final_w + 16 * lane))[i];
;             ((f32x4*)orow)[i] = (f32x4){xo[i].x * rstd3 * w.x, xo[i].y * rstd3 * w.y, xo[i].z * rstd3 * w.z, xo[i].w * rstd3 * w.w}; }
	v_pk_fma_f32 v[34:35], v[94:95], v[48:49], v[34:35] op_sel_hi:[1,0,1]
	v_pk_fma_f32 v[30:31], v[98:99], v[48:49], v[30:31] op_sel_hi:[1,0,1]
	v_pk_fma_f32 v[28:29], v[100:101], v[48:49], v[28:29] op_sel_hi:[1,0,1]
	v_pk_fma_f32 v[32:33], v[96:97], v[48:49], v[32:33] op_sel_hi:[1,0,1]
	v_pk_mul_f32 v[36:37], v[152:153], v[42:43]
	v_pk_mul_f32 v[38:39], v[154:155], v[40:41]
	global_store_dwordx4 v[56:57], v[36:39], off offset:48
	s_nop 0
	v_lshlrev_b32_e32 v50, 16, v164
	v_and_b32_e32 v51, 0xffff0000, v164
	v_lshlrev_b32_e32 v36, 16, v165
	v_and_b32_e32 v37, 0xffff0000, v165
	v_lshlrev_b32_e32 v52, 16, v166
	v_and_b32_e32 v53, 0xffff0000, v166
	v_lshlrev_b32_e32 v38, 16, v167
	v_and_b32_e32 v39, 0xffff0000, v167
	v_lshlrev_b32_e32 v56, 16, v168
	v_and_b32_e32 v57, 0xffff0000, v168
	v_lshlrev_b32_e32 v40, 16, v169
	v_and_b32_e32 v41, 0xffff0000, v169
	v_lshlrev_b32_e32 v58, 16, v170
	v_and_b32_e32 v59, 0xffff0000, v170
	v_lshlrev_b32_e32 v42, 16, v171
	v_and_b32_e32 v43, 0xffff0000, v171
	v_pk_add_f32 v[20:21], v[20:21], v[50:51]
	v_pk_add_f32 v[22:23], v[22:23], v[36:37]
	v_pk_add_f32 v[24:25], v[24:25], v[52:53]
	v_pk_add_f32 v[26:27], v[26:27], v[38:39]
	v_pk_add_f32 v[28:29], v[28:29], v[56:57]
	v_pk_add_f32 v[30:31], v[30:31], v[40:41]
	v_pk_add_f32 v[34:35], v[34:35], v[42:43]
	v_pk_mul_f32 v[36:37], v[20:21], v[20:21]
	v_pk_mul_f32 v[38:39], v[22:23], v[22:23]
	v_pk_mul_f32 v[40:41], v[24:25], v[24:25]
	v_pk_mul_f32 v[42:43], v[26:27], v[26:27]
	v_pk_add_f32 v[32:33], v[32:33], v[58:59]
	v_pk_mul_f32 v[50:51], v[28:29], v[28:29]
	v_pk_mul_f32 v[52:53], v[30:31], v[30:31]
	v_add_f32_e32 v42, v42, v43
	v_add_f32_e32 v40, v40, v41
	v_add_f32_e32 v38, v38, v39
	v_add_f32_e32 v36, v36, v37
	v_pk_mul_f32 v[56:57], v[32:33], v[32:33]
	v_pk_mul_f32 v[58:59], v[34:35], v[34:35]
	v_add_f32_e32 v37, v52, v53
	v_add_f32_e32 v39, v50, v51
	v_add_f32_e32 v40, v40, v42
	v_add_f32_e32 v36, v36, v38
	v_add_f32_e32 v41, v58, v59
	v_add_f32_e32 v43, v56, v57
	v_add_f32_e32 v37, v39, v37
	v_add_f32_e32 v36, v36, v40
	v_add_f32_e32 v38, v43, v41
	v_add_f32_e32 v36, v36, v37
	v_add_f32_e32 v36, v38, v36
	s_nop 1
	v_add_f32_dpp v36, v36, v36 quad_perm:[1,0,3,2] row_mask:0xf bank_mask:0xf bound_ctrl:1
	s_nop 1
	v_add_f32_dpp v36, v36, v36 quad_perm:[2,3,0,1] row_mask:0xf bank_mask:0xf bound_ctrl:1
	s_nop 1
	v_add_f32_dpp v36, v36, v36 row_half_mirror row_mask:0xf bank_mask:0xf bound_ctrl:1
	s_nop 1
	v_add_f32_dpp v36, v36, v36 row_mirror row_mask:0xf bank_mask:0xf bound_ctrl:1
	v_mov_b32_e32 v37, v36
	s_nop 1
	v_permlane16_swap_b32_e32 v36, v37
	v_add_f32 v36, v36, v37
	s_nop 1
	s_nop 0
	v_mov_b32_e32 v37, v36
	s_nop 1
	v_permlane32_swap_b32_e32 v36, v37
	v_add_f32 v36, v36, v37
	s_nop 0
	v_fmamk_f32 v36, v36, 0x3a800000, v110
	v_mul_f32_e32 v37, 0x4b800000, v36
	v_cmp_gt_f32_e64 s[0:1], s8, v36
	s_nop 1
	v_cndmask_b32_e64 v36, v36, v37, s[0:1]
	v_rsq_f32_e32 v38, v36
	v_lshl_add_u64 v[36:37], v[54:55], 0, s[2:3]
	v_mul_f32_e32 v39, 0x45800000, v38
	v_cndmask_b32_e64 v38, v38, v39, s[0:1]
	v_pk_mul_f32 v[20:21], v[20:21], v[38:39] op_sel_hi:[1,0]
	v_pk_mul_f32 v[22:23], v[22:23], v[38:39] op_sel_hi:[1,0]
	v_pk_mul_f32 v[20:21], v[140:141], v[20:21]
	v_pk_mul_f32 v[22:23], v[142:143], v[22:23]
	global_store_dwordx4 v[36:37], v[20:23], off
	v_pk_mul_f32 v[26:27], v[26:27], v[38:39] op_sel_hi:[1,0]
	v_pk_mul_f32 v[24:25], v[24:25], v[38:39] op_sel_hi:[1,0]
	s_add_i32 s0, s84, 3
	s_ashr_i32 s1, s0, 31
	s_lshl_b64 s[2:3], s[0:1], 11
	s_lshl_b64 s[0:1], s[0:1], 12
	v_pk_mul_f32 v[20:21], v[144:145], v[24:25]
	v_pk_mul_f32 v[22:23], v[146:147], v[26:27]
	global_store_dwordx4 v[36:37], v[20:23], off offset:16
	v_pk_mul_f32 v[24:25], v[30:31], v[38:39] op_sel_hi:[1,0]
	v_pk_mul_f32 v[26:27], v[28:29], v[38:39] op_sel_hi:[1,0]
	v_lshl_add_u64 v[28:29], v[72:73], 0, s[2:3]
	v_pk_mul_f32 v[20:21], v[148:149], v[26:27]
	v_pk_mul_f32 v[22:23], v[150:151], v[24:25]
	global_store_dwordx4 v[36:37], v[20:23], off offset:32
	v_pk_mul_f32 v[24:25], v[34:35], v[38:39] op_sel_hi:[1,0]
	v_pk_mul_f32 v[26:27], v[32:33], v[38:39] op_sel_hi:[1,0]
	v_cndmask_b32_e32 v32, 0, v117, vcc
	v_pk_fma_f32 v[0:1], v[0:1], v[32:33], v[18:19] op_sel_hi:[1,0,1]
	v_pk_fma_f32 v[2:3], v[2:3], v[32:33], v[16:17] op_sel_hi:[1,0,1]
; #define LDS_WAIT() asm volatile("s_waitcnt lgkmcnt(0)" ::: "memory")
;     ...
; #pragma unroll
;     for (int j = 0; j < PE_NT; ++j) {
;         const int t = tbase + j;
;         float ss = 0.f; f32x4 xo[4];
;         { const v4u* xrow = (const v4u*)((const bf16*)(ws + WS_XB) + (size_t)t * 1024 + 16 * lane); const v4u xa = xrow[0], xc = xrow[1];
;           xo[0] = (f32x4){bflo(xa.x), bfhi(xa.x), bflo(xa.y), bfhi(xa.y)}; xo[1] = (f32x4){bflo(xa.z), bfhi(xa.z), bflo(xa.w), bfhi(xa.w)};
;           xo[2] = (f32x4){bflo(xc.x), bfhi(xc.x), bflo(xc.y), bfhi(xc.y)}; xo[3] = (f32x4){bflo(xc.z), bfhi(xc.z), bflo(xc.w), bfhi(xc.w)}; }
; #pragma unroll
;         for (int i = 0; i < 4; ++i) { xo[i].x += acc[j][2 * i].x; xo[i].y += acc[j][2 * i].y; xo[i].z += acc[j][2 * i + 1].x; xo[i].w += acc[j][2 * i + 1].y;
;             ss += (xo[i].x * xo[i].x + xo[i].y * xo[i].y) + (xo[i].z * xo[i].z + xo[i].w * xo[i].w); }
;         const float rstd3 = rsqrtf(wave_sum(ss) * (1.0f / 1024.0f) + 1e-6f);
;         float* orow = dstbase + (size_t)t * 1024 + 16 * lane;
; #pragma unroll
;         for (int i = 0; i < 4; ++i) { const f32x4 w = ((const f32x4*)(P.norm_final_w + 16 * lane))[i];
;             ((f32x4*)orow)[i] = (f32x4){xo[i].x * rstd3 * w.x, xo[i].y * rstd3 * w.y, xo[i].z * rstd3 * w.z, xo[i].w * rstd3 * w.w}; }
;     }
;     LDS_WAIT(); asm volatile("s_waitcnt vmcnt(0)" ::: "memory");
	v_pk_fma_f32 v[14:15], v[104:105], v[32:33], v[14:15] op_sel_hi:[1,0,1]
	v_pk_fma_f32 v[12:13], v[102:103], v[32:33], v[12:13] op_sel_hi:[1,0,1]
	v_pk_fma_f32 v[10:11], v[100:101], v[32:33], v[10:11] op_sel_hi:[1,0,1]
	v_pk_fma_f32 v[8:9], v[98:99], v[32:33], v[8:9] op_sel_hi:[1,0,1]
	v_pk_fma_f32 v[6:7], v[96:97], v[32:33], v[6:7] op_sel_hi:[1,0,1]
	v_pk_fma_f32 v[4:5], v[94:95], v[32:33], v[4:5] op_sel_hi:[1,0,1]
	v_pk_mul_f32 v[20:21], v[152:153], v[26:27]
	v_pk_mul_f32 v[22:23], v[154:155], v[24:25]
	global_store_dwordx4 v[36:37], v[20:23], off offset:48
	s_nop 0
	v_lshlrev_b32_e32 v16, 16, v172
	v_and_b32_e32 v17, 0xffff0000, v172
	v_lshlrev_b32_e32 v18, 16, v173
	v_and_b32_e32 v19, 0xffff0000, v173
	v_lshlrev_b32_e32 v20, 16, v174
	v_and_b32_e32 v21, 0xffff0000, v174
	v_lshlrev_b32_e32 v22, 16, v175
	v_and_b32_e32 v23, 0xffff0000, v175
	v_lshlrev_b32_e32 v32, 16, v176
	v_and_b32_e32 v33, 0xffff0000, v176
	v_lshlrev_b32_e32 v24, 16, v177
	v_and_b32_e32 v25, 0xffff0000, v177
	v_pk_add_f32 v[0:1], v[0:1], v[16:17]
	v_pk_add_f32 v[2:3], v[2:3], v[18:19]
	v_pk_add_f32 v[14:15], v[14:15], v[20:21]
	v_pk_add_f32 v[12:13], v[12:13], v[22:23]
	v_lshlrev_b32_e32 v34, 16, v178
	v_and_b32_e32 v35, 0xffff0000, v178
	v_lshlrev_b32_e32 v26, 16, v179
	v_and_b32_e32 v27, 0xffff0000, v179
	v_pk_add_f32 v[10:11], v[10:11], v[32:33]
	v_pk_add_f32 v[8:9], v[8:9], v[24:25]
	v_pk_mul_f32 v[16:17], v[0:1], v[0:1]
	v_pk_mul_f32 v[18:19], v[2:3], v[2:3]
	v_pk_mul_f32 v[20:21], v[14:15], v[14:15]
	v_pk_mul_f32 v[22:23], v[12:13], v[12:13]
	v_pk_add_f32 v[6:7], v[6:7], v[34:35]
	v_pk_add_f32 v[4:5], v[4:5], v[26:27]
	v_pk_mul_f32 v[24:25], v[10:11], v[10:11]
	v_pk_mul_f32 v[26:27], v[8:9], v[8:9]
	v_add_f32_e32 v22, v22, v23
	v_add_f32_e32 v20, v20, v21
	v_add_f32_e32 v18, v18, v19
	v_add_f32_e32 v16, v16, v17
	v_pk_mul_f32 v[32:33], v[6:7], v[6:7]
	v_pk_mul_f32 v[34:35], v[4:5], v[4:5]
	v_add_f32_e32 v17, v26, v27
	v_add_f32_e32 v19, v24, v25
	v_add_f32_e32 v20, v20, v22
	v_add_f32_e32 v16, v16, v18
	v_add_f32_e32 v21, v34, v35
	v_add_f32_e32 v23, v32, v33
	v_add_f32_e32 v17, v19, v17
	v_add_f32_e32 v16, v16, v20
	v_add_f32_e32 v18, v23, v21
	v_add_f32_e32 v16, v16, v17
	v_add_f32_e32 v16, v18, v16
	s_nop 1
	v_add_f32_dpp v16, v16, v16 quad_perm:[1,0,3,2] row_mask:0xf bank_mask:0xf bound_ctrl:1
	s_nop 1
	v_add_f32_dpp v16, v16, v16 quad_perm:[2,3,0,1] row_mask:0xf bank_mask:0xf bound_ctrl:1
	s_nop 1
	v_add_f32_dpp v16, v16, v16 row_half_mirror row_mask:0xf bank_mask:0xf bound_ctrl:1
	s_nop 1
	v_add_f32_dpp v16, v16, v16 row_mirror row_mask:0xf bank_mask:0xf bound_ctrl:1
	v_mov_b32_e32 v17, v16
	s_nop 1
	v_permlane16_swap_b32_e32 v16, v17
	v_add_f32 v16, v16, v17
	s_nop 1
	s_nop 0
	v_mov_b32_e32 v17, v16
	s_nop 1
	v_permlane32_swap_b32_e32 v16, v17
	v_add_f32 v16, v16, v17
	s_nop 0
	v_fmamk_f32 v16, v16, 0x3a800000, v110
	v_mul_f32_e32 v17, 0x4b800000, v16
	v_cmp_gt_f32_e32 vcc, s8, v16
	s_nop 1
	v_cndmask_b32_e32 v16, v16, v17, vcc
	v_rsq_f32_e32 v18, v16
	v_lshl_add_u64 v[16:17], v[54:55], 0, s[0:1]
	v_readlane_b32 s0, v255, 4
	s_add_i32 s6, s6, s0
	v_mul_f32_e32 v19, 0x45800000, v18
	v_cndmask_b32_e32 v18, v18, v19, vcc
	v_pk_mul_f32 v[0:1], v[0:1], v[18:19] op_sel_hi:[1,0]
	v_pk_mul_f32 v[2:3], v[2:3], v[18:19] op_sel_hi:[1,0]
	v_pk_mul_f32 v[0:1], v[140:141], v[0:1]
	v_pk_mul_f32 v[2:3], v[142:143], v[2:3]
	global_store_dwordx4 v[16:17], v[0:3], off
	v_pk_mul_f32 v[12:13], v[12:13], v[18:19] op_sel_hi:[1,0]
	v_pk_mul_f32 v[14:15], v[14:15], v[18:19] op_sel_hi:[1,0]
	v_pk_mul_f32 v[8:9], v[8:9], v[18:19] op_sel_hi:[1,0]
	v_pk_mul_f32 v[10:11], v[10:11], v[18:19] op_sel_hi:[1,0]
	v_pk_mul_f32 v[4:5], v[4:5], v[18:19] op_sel_hi:[1,0]
	v_pk_mul_f32 v[6:7], v[6:7], v[18:19] op_sel_hi:[1,0]
	s_cmpk_lt_i32 s6, 0x4000
	v_pk_mul_f32 v[0:1], v[144:145], v[14:15]
	v_pk_mul_f32 v[2:3], v[146:147], v[12:13]
	global_store_dwordx4 v[16:17], v[0:3], off offset:16
	s_nop 1
	v_pk_mul_f32 v[0:1], v[148:149], v[10:11]
	v_pk_mul_f32 v[2:3], v[150:151], v[8:9]
	global_store_dwordx4 v[16:17], v[0:3], off offset:32
	s_nop 1
	v_pk_mul_f32 v[0:1], v[152:153], v[6:7]
	v_pk_mul_f32 v[2:3], v[154:155], v[4:5]
	global_store_dwordx4 v[16:17], v[0:3], off offset:48
	s_waitcnt lgkmcnt(0)
	s_cbranch_scc0 .LBB0_2885
